# stick-breaking units assigned statically and paired against the MLA units (unit = 255 - workgroup id): a workgroup with a long MLA unit gets a short stick-breaking unit; no device-atomic claims for ei
# speedup vs baseline: 1.0047x; 1.0008x over previous
; __device__ __forceinline__ void claim_fire(unsigned* ctr, int tid, int* pend) { if (tid == 0) *pend = (int)__hip_atomic_fetch_add(ctr, 1u, __ATOMIC_RELAXED, __HIP_MEMORY_SCOPE_AGENT); }
;     ...
;     at::claim_fire(q3ctr, F.tid, &pend);
;     ...
;         const int idx = at::claim_take(lds, F.tid, &pend); if (idx >= 256) break;
;         const int qb = 31 - (idx >> 3), bh = idx & 7, b = bh >> 2, h = bh & 3;
.LBB0_992:
	s_load_dwordx2 s[10:11], s[46:47], 0x38
	s_and_saveexec_b64 s[14:15], s[38:39]
	s_cbranch_execz .LBB0_996
	s_mov_b64 s[34:35], exec
	v_mbcnt_lo_u32_b32 v0, s34, 0
	v_mbcnt_hi_u32_b32 v0, s35, v0
	v_cmp_eq_u32_e32 vcc, 0, v0
	s_and_saveexec_b64 s[16:17], vcc
	s_cbranch_execz .LBB0_995
	s_sub_i32 s3, 0xff, s92
	v_mov_b32_e32 v1, s3
	s_nop 0

; __device__ __forceinline__ void sb_unit(LAS unsigned char* lds, int wv, int lane, const Tens T, int q0, bf16_t* outp, int opitch, unsigned* nctr, int* pend) {
;     ...
;     if (tid == 0) *pend = (int)__hip_atomic_fetch_add(nctr, 1u, __ATOMIC_RELAXED, __HIP_MEMORY_SCOPE_AGENT);
;     ...
;         const int idx = at::claim_take(lds, F.tid, &pend); if (idx >= 256) break;
.LBB0_1016:
	v_cmp_eq_u32_e32 vcc, 0, v140
	s_and_saveexec_b64 s[16:17], vcc
	s_cbranch_execz .LBB0_998
	s_mov_b64 s[40:41], exec
	v_mbcnt_lo_u32_b32 v16, s40, 0
	v_mbcnt_hi_u32_b32 v16, s41, v16
	v_cmp_eq_u32_e32 vcc, 0, v16
	s_and_saveexec_b64 s[34:35], vcc
	s_cbranch_execz .LBB0_997
	s_bcnt1_i32_b64 s20, s[40:41]
	v_mov_b32_e32 v17, s20
	v_mov_b32_e32 v192, 0x100
	s_branch .LBB0_997
